# LN2 row loop: the 8 loop-invariant gamma/beta loads per row loaded once before the loop (register moves in the loop)
# baseline (speedup 1.0000x reference)
; #define GAS __attribute__((address_space(1)))
; __device__ __forceinline__ void ph_ln2(Frame& F, int l, int ntok, bool last) {
;     const int gw = F.wg * NWAVES + F.wave, NGW = F.G * NWAVES;
;     const int cA = 256 * (F.lane >> 4) + 32 * ((F.lane >> 2) & 3) + 8 * (F.lane & 3);
;     ...
;     const float* lg = F.in[I_LN2G] + l * DM; const float* lb = F.in[I_LN2B] + l * DM;
;     struct Ln2Raw { u32x2 q[8]; u32x4 qs, xa, xb; };
;     auto ln2_load = [&](int row) { Ln2Raw r;
;         const unsigned char* y2 = (const unsigned char*)(F.ws + WS_Y2) + (size_t)row * 5120;
;         const bf16_t* xr = (const bf16_t*)(F.ws + WS_XR) + (size_t)row * DM;
; #pragma unroll
;         for (int k = 0; k < 8; ++k) r.q[k] = __builtin_nontemporal_load((const GAS u32x2*)(y2 + k * 512 + 8 * F.lane));
;         r.qs = __builtin_nontemporal_load((const GAS u32x4*)(y2 + 4096 + 16 * F.lane));
;         r.xa = __builtin_nontemporal_load((const GAS u32x4*)(xr + cA)); r.xb = __builtin_nontemporal_load((const GAS u32x4*)(xr + cA + 128));
;         return r; };
;     Ln2Raw cur = ln2_load(gw < ntok ? gw : 0);
.LBB0_1687:
	v_readlane_b32 s36, v252, 8
	s_mov_b32 s0, s97
	v_readlane_b32 s38, v252, 10
	v_readlane_b32 s39, v252, 11
	v_readlane_b32 s4, v254, 28
	v_mbcnt_lo_u32_b32 v8, -1, 0
	v_mbcnt_hi_u32_b32 v8, -1, v8
	v_readlane_b32 s37, v252, 9
	s_mov_b64 s[20:21], s[38:39]
	s_add_i32 s38, s0, s4
	s_mov_b64 s[2:3], s[36:37]
	s_cmp_ge_i32 s38, s80
	s_cbranch_scc1 .LBB0_1696
	s_lshl_b32 s22, s30, 10
	v_readlane_b32 s40, v252, 0
	s_lshl_b64 s[4:5], s[22:23], 2
	v_readlane_b32 s46, v252, 6
	v_readlane_b32 s47, v252, 7
	s_add_u32 s18, s46, s4
	v_readlane_b32 s44, v252, 4
	s_addc_u32 s19, s47, s5
	v_readlane_b32 s45, v252, 5
	s_add_u32 s4, s44, s4
	s_addc_u32 s5, s45, s5
	s_add_u32 s36, s20, 0x64000000
	v_lshlrev_b32_e32 v34, 3, v8
	v_readlane_b32 s42, v252, 2
	v_readlane_b32 s43, v252, 3
	s_addc_u32 s37, s21, 0
	s_ashr_i32 s39, s38, 31
	v_lshlrev_b32_e32 v32, 4, v8
	v_and_b32_e32 v0, 0x78, v34
	s_movk_i32 s0, 0xff00
	s_lshl_b64 s[42:43], s[38:39], 11
	v_and_or_b32 v36, v32, s0, v0
	v_readlane_b32 s41, v252, 1
	s_add_u32 s40, s36, s42
	v_ashrrev_i32_e32 v37, 31, v36
	s_addc_u32 s41, s37, s43
	v_lshlrev_b64 v[10:11], 1, v[36:37]
	s_add_u32 s22, s20, 0x2f600000
	v_lshl_add_u64 v[0:1], s[40:41], 0, v[10:11]
	s_addc_u32 s44, s21, 0
	s_mul_i32 s40, s38, 0x1400
	s_mul_hi_i32 s0, s38, 0x1400
	s_add_u32 s40, s22, s40
	s_addc_u32 s41, s44, s0
	v_ashrrev_i32_e32 v33, 31, v32
	s_waitcnt vmcnt(0)
	v_lshl_add_u64 v[4:5], s[40:41], 0, v[32:33]
	s_movk_i32 s0, 0x1000
	v_add_co_u32_e32 v4, vcc, s0, v4
	v_ashrrev_i32_e32 v35, 31, v34
	s_nop 0
	v_addc_co_u32_e32 v5, vcc, 0, v5, vcc
	v_lshl_add_u64 v[16:17], s[40:41], 0, v[34:35]
	global_load_dwordx4 v[12:15], v[0:1], off offset:256 nt
	s_nop 0
	global_load_dwordx4 v[0:3], v[0:1], off nt
	s_nop 0
	global_load_dwordx2 v[66:67], v[16:17], off offset:3584 nt
	global_load_dwordx2 v[64:65], v[16:17], off offset:3072 nt
	global_load_dwordx2 v[62:63], v[16:17], off offset:2560 nt
	global_load_dwordx2 v[60:61], v[16:17], off offset:2048 nt
	global_load_dwordx2 v[58:59], v[16:17], off offset:1536 nt
	global_load_dwordx2 v[56:57], v[16:17], off offset:1024 nt
	global_load_dwordx2 v[54:55], v[16:17], off offset:512 nt
	s_nop 0
	global_load_dwordx4 v[4:7], v[4:5], off nt
	s_nop 0
	global_load_dwordx2 v[52:53], v[16:17], off nt
	s_mul_i32 s45, s30, 17
	s_add_i32 s46, s45, 17
	v_lshlrev_b64 v[40:41], 2, v[36:37]
	s_add_u32 s47, s20, 0x100000
	v_lshl_add_u64 v[42:43], s[4:5], 0, v[40:41]
	s_addc_u32 s48, s21, 0
	s_lshl_b64 s[40:41], s[38:39], 5
	s_lshl_b64 s[4:5], s[38:39], 12
	s_add_u32 s2, s2, s4
	v_or_b32_e32 v38, 0x80, v36
	v_lshlrev_b32_e32 v8, 2, v8
	s_addc_u32 s3, s3, s5
	v_ashrrev_i32_e32 v39, 31, v38
	v_lshl_add_u64 v[44:45], s[18:19], 0, v[40:41]
	v_lshl_add_u64 v[46:47], s[36:37], 0, v[10:11]
	v_xor_b32_e32 v103, 4, v8
	v_xor_b32_e32 v107, 8, v8
	v_xor_b32_e32 v113, 16, v8
	v_xor_b32_e32 v170, 32, v8
	v_xor_b32_e32 v171, 64, v8
	v_xor_b32_e32 v172, 0x80, v8
	v_lshl_add_u64 v[48:49], s[2:3], 0, v[40:41]
	v_lshl_add_u64 v[50:51], s[42:43], 0, v[10:11]
	global_load_dwordx4 v[182:185], v[42:43], off offset:16
	global_load_dwordx4 v[186:189], v[42:43], off
	global_load_dwordx4 v[194:197], v[44:45], off offset:16
	global_load_dwordx4 v[198:201], v[44:45], off
	global_load_dwordx4 v[202:205], v[42:43], off offset:528
	global_load_dwordx4 v[216:219], v[42:43], off offset:512
	global_load_dwordx4 v[220:223], v[44:45], off offset:528
	global_load_dwordx4 v[236:239], v[44:45], off offset:512
	s_branch .LBB0_1690

; #define GAS __attribute__((address_space(1)))
; __device__ __forceinline__ unsigned pk2(float lo, float hi) { const f32x2 v = {lo, hi}; const bf16v2 b = __builtin_convertvector(v, bf16v2); return __builtin_bit_cast(unsigned, b); }
; __device__ __forceinline__ const float* mod_ptr(const Frame& F, int l, int row) { return (const float*)(F.ws + WS_MOD) + ((size_t)l * 17 + row_b(row)) * 6144; }
; __device__ __forceinline__ void ph_ln2(Frame& F, int l, int ntok, bool last) {
;     ...
;         const float rstd = 1.f / sqrtf(wave_sum(s2, F.lane) * (1.f / DM) + LN_EPS);
;         const float* mdn = last ? md : mod_ptr(F, l + 1, row);
;         float xn[16];
; #pragma unroll
;         for (int j = 0; j < 4; ++j) { const f32x4 g = *(const GAS f32x4*)(lg + LN2_COL(j)), bb = *(const GAS f32x4*)(lb + LN2_COL(j));
; #pragma unroll
;             for (int e = 0; e < 4; ++e) xn[4 * j + e] = v[4 * j + e] * rstd * g[e] + bb[e]; }
;         if (last) { float* op = F.out + (size_t)row * DM;
; #pragma unroll
;             for (int j = 0; j < 4; ++j) *(GAS f32x4*)(op + LN2_COL(j)) = (f32x4){xn[4 * j], xn[4 * j + 1], xn[4 * j + 2], xn[4 * j + 3]}; }
;         else {
;             __builtin_nontemporal_store((u32x4){pk2(xn[0], xn[1]), pk2(xn[2], xn[3]), pk2(xn[4], xn[5]), pk2(xn[6], xn[7])}, (GAS u32x4*)(xr + cA)); __builtin_nontemporal_store((u32x4){pk2(xn[8], xn[9]), pk2(xn[10], xn[11]), pk2(xn[12], xn[13]), pk2(xn[14], xn[15])}, (GAS u32x4*)(xr + cA + 128));
;             bf16_t* xm = (bf16_t*)(F.ws + WS_XM) + (size_t)row * DM;
;             unsigned w[8];
; #pragma unroll
;             for (int j = 0; j < 4; ++j) { const f32x4 sh = *(const GAS f32x4*)(mdn + LN2_COL(j)), sc = *(const GAS f32x4*)(mdn + 1024 + LN2_COL(j));
;                 w[2 * j] = pk2(xn[4 * j] * (1.f + sc[0]) + sh[0], xn[4 * j + 1] * (1.f + sc[1]) + sh[1]); w[2 * j + 1] = pk2(xn[4 * j + 2] * (1.f + sc[2]) + sh[2], xn[4 * j + 3] * (1.f + sc[3]) + sh[3]); }
;             *(GAS u32x4*)(xm + cA) = (u32x4){w[0], w[1], w[2], w[3]}; *(GAS u32x4*)(xm + cA + 128) = (u32x4){w[4], w[5], w[6], w[7]};
.LBB0_1692:
	s_waitcnt lgkmcnt(0)
	v_add_f32_e32 v16, v16, v17
	v_fmamk_f32 v16, v16, 0x3a800000, v234
	s_mov_b32 s0, 0xf800000
	v_cmp_gt_f32_e32 vcc, s0, v16
	v_mul_f32_e32 v17, 0x4f800000, v16
	s_nop 0
	v_cndmask_b32_e32 v16, v16, v17, vcc
	v_sqrt_f32_e32 v17, v16
	s_nop 0
	v_add_u32_e32 v18, -1, v17
	v_fma_f32 v19, -v18, v17, v16
	v_cmp_ge_f32_e64 s[36:37], 0, v19
	v_add_u32_e32 v19, 1, v17
	s_nop 0
	v_cndmask_b32_e64 v18, v17, v18, s[36:37]
	v_fma_f32 v17, -v19, v17, v16
	v_cmp_lt_f32_e64 s[36:37], 0, v17
	s_nop 1
	v_cndmask_b32_e64 v17, v18, v19, s[36:37]
	v_mul_f32_e32 v18, 0x37800000, v17
	v_cndmask_b32_e32 v17, v17, v18, vcc
	v_cmp_class_f32_e32 vcc, v16, v232
	s_mov_b64 s[36:37], -1
	s_nop 0
	v_cndmask_b32_e32 v16, v17, v16, vcc
	v_div_scale_f32 v17, s[4:5], v16, v16, 1.0
	v_rcp_f32_e32 v18, v17
	v_readlane_b32 s4, v255, 32
	v_readlane_b32 s5, v255, 33
	v_fma_f32 v19, -v17, v18, 1.0
	v_fmac_f32_e32 v18, v19, v18
	v_div_scale_f32 v19, vcc, 1.0, v16, 1.0
	v_mul_f32_e32 v68, v19, v18
	v_fma_f32 v69, -v17, v68, v19
	v_fmac_f32_e32 v68, v69, v18
	v_fma_f32 v17, -v17, v68, v19
	v_div_fmas_f32 v17, v17, v18, v68
	v_div_fixup_f32 v80, v17, v16, 1.0
	v_mov_b32_e32 v68, v182
	v_mov_b32_e32 v69, v183
	v_mov_b32_e32 v70, v184
	v_mov_b32_e32 v71, v185
	v_mov_b32_e32 v16, v186
	v_mov_b32_e32 v17, v187
	v_mov_b32_e32 v18, v188
	v_mov_b32_e32 v19, v189
	v_mov_b32_e32 v72, v194
	v_mov_b32_e32 v73, v195
	v_mov_b32_e32 v74, v196
	v_mov_b32_e32 v75, v197
	v_mov_b32_e32 v76, v198
	v_mov_b32_e32 v77, v199
	v_mov_b32_e32 v78, v200
	v_mov_b32_e32 v79, v201
	v_pk_mul_f32 v[12:13], v[12:13], v[80:81] op_sel_hi:[1,0]
	v_pk_mul_f32 v[20:21], v[20:21], v[80:81] op_sel_hi:[1,0]
	s_and_b64 vcc, exec, s[4:5]
	s_waitcnt vmcnt(0)
	v_pk_fma_f32 v[16:17], v[12:13], v[16:17], v[76:77]
	v_pk_mul_f32 v[12:13], v[14:15], v[80:81] op_sel_hi:[1,0]
	v_pk_mul_f32 v[14:15], v[26:27], v[80:81] op_sel_hi:[1,0]
	v_pk_fma_f32 v[18:19], v[12:13], v[18:19], v[78:79]
	v_pk_mul_f32 v[12:13], v[24:25], v[80:81] op_sel_hi:[1,0]
	v_pk_fma_f32 v[14:15], v[14:15], v[70:71], v[74:75]
	v_pk_fma_f32 v[12:13], v[12:13], v[68:69], v[72:73]
	v_mov_b32_e32 v68, v202
	v_mov_b32_e32 v69, v203
	v_mov_b32_e32 v70, v204
	v_mov_b32_e32 v71, v205
	v_mov_b32_e32 v24, v216
	v_mov_b32_e32 v25, v217
	v_mov_b32_e32 v26, v218
	v_mov_b32_e32 v27, v219
	v_mov_b32_e32 v72, v220
	v_mov_b32_e32 v73, v221
	v_mov_b32_e32 v74, v222
	v_mov_b32_e32 v75, v223
	v_mov_b32_e32 v76, v236
	v_mov_b32_e32 v77, v237
	v_mov_b32_e32 v78, v238
	v_mov_b32_e32 v79, v239
	s_waitcnt vmcnt(0)
	v_pk_fma_f32 v[24:25], v[20:21], v[24:25], v[76:77]
	v_pk_mul_f32 v[20:21], v[22:23], v[80:81] op_sel_hi:[1,0]
	v_pk_mul_f32 v[22:23], v[30:31], v[80:81] op_sel_hi:[1,0]
	v_pk_fma_f32 v[26:27], v[20:21], v[26:27], v[78:79]
	v_pk_mul_f32 v[20:21], v[28:29], v[80:81] op_sel_hi:[1,0]
	v_pk_fma_f32 v[22:23], v[22:23], v[70:71], v[74:75]
	v_pk_fma_f32 v[20:21], v[20:21], v[68:69], v[72:73]
	s_cbranch_vccz .LBB0_1694
	v_lshl_add_u64 v[84:85], s[20:21], 0, v[50:51]
	v_add_co_u32_e32 v68, vcc, 0x64000000, v84
	v_cvt_pk_bf16_f32 v28, v16, v17
	v_cvt_pk_bf16_f32 v29, v18, v19
	v_cvt_pk_bf16_f32 v30, v12, v13
	v_cvt_pk_bf16_f32 v31, v14, v15
	v_addc_co_u32_e32 v69, vcc, 0, v85, vcc
	s_add_u32 s36, s2, 0x1000
	global_store_dwordx4 v[68:69], v[28:31], off nt
	s_addc_u32 s37, s3, 0
	v_lshl_add_u64 v[80:81], s[2:3], 0, v[40:41]
	v_cvt_pk_bf16_f32 v28, v24, v25
	v_cvt_pk_bf16_f32 v29, v26, v27
	v_cvt_pk_bf16_f32 v30, v20, v21
	v_cvt_pk_bf16_f32 v31, v22, v23
	global_store_dwordx4 v[68:69], v[28:31], off offset:256 nt
	v_lshl_add_u64 v[76:77], s[36:37], 0, v[40:41]
	global_load_dwordx4 v[68:71], v[80:81], off offset:16
	global_load_dwordx4 v[28:31], v[80:81], off
	global_load_dwordx4 v[72:75], v[76:77], off offset:16
	s_nop 0
	global_load_dwordx4 v[76:79], v[76:77], off
	s_waitcnt vmcnt(0)
	v_pk_add_f32 v[76:77], v[76:77], 1.0 op_sel_hi:[1,0]
	s_nop 0
	v_pk_fma_f32 v[28:29], v[16:17], v[76:77], v[28:29]
	v_pk_add_f32 v[76:77], v[78:79], 1.0 op_sel_hi:[1,0]
	v_cvt_pk_bf16_f32 v28, v28, v29
	v_pk_fma_f32 v[30:31], v[18:19], v[76:77], v[30:31]
	s_nop 0
	v_cvt_pk_bf16_f32 v29, v30, v31
	v_pk_add_f32 v[30:31], v[72:73], 1.0 op_sel_hi:[1,0]
	s_nop 0
	v_pk_fma_f32 v[30:31], v[12:13], v[30:31], v[68:69]
	v_pk_add_f32 v[68:69], v[74:75], 1.0 op_sel_hi:[1,0]
	v_cvt_pk_bf16_f32 v30, v30, v31
	v_pk_fma_f32 v[68:69], v[14:15], v[68:69], v[70:71]
	s_nop 0
	v_cvt_pk_bf16_f32 v31, v68, v69
	global_load_dwordx4 v[68:71], v[80:81], off offset:528
	global_load_dwordx4 v[72:75], v[80:81], off offset:512
	v_lshl_add_u64 v[80:81], v[38:39], 2, s[36:37]
	global_load_dwordx4 v[76:79], v[80:81], off offset:16
	s_nop 0
	global_load_dwordx4 v[80:83], v[80:81], off
	s_mov_b64 s[36:37], 0
	s_waitcnt vmcnt(0)
	v_pk_add_f32 v[80:81], v[80:81], 1.0 op_sel_hi:[1,0]
	s_nop 0
	v_pk_fma_f32 v[72:73], v[24:25], v[80:81], v[72:73]
	v_pk_add_f32 v[80:81], v[82:83], 1.0 op_sel_hi:[1,0]
	v_cvt_pk_bf16_f32 v72, v72, v73
	v_pk_fma_f32 v[74:75], v[26:27], v[80:81], v[74:75]
	s_nop 0
	v_cvt_pk_bf16_f32 v73, v74, v75
	v_pk_add_f32 v[74:75], v[76:77], 1.0 op_sel_hi:[1,0]
	s_nop 0
	v_pk_fma_f32 v[68:69], v[20:21], v[74:75], v[68:69]
	s_nop 0
	v_cvt_pk_bf16_f32 v74, v68, v69
	v_pk_add_f32 v[68:69], v[78:79], 1.0 op_sel_hi:[1,0]
	s_nop 0
	v_pk_fma_f32 v[68:69], v[22:23], v[68:69], v[70:71]
	s_nop 0
	v_cvt_pk_bf16_f32 v75, v68, v69
	v_add_co_u32_e32 v68, vcc, 0x11b00000, v84
	s_nop 1
	v_addc_co_u32_e32 v69, vcc, 0, v85, vcc
	global_store_dwordx4 v[68:69], v[28:31], off
	global_store_dwordx4 v[68:69], v[72:75], off offset:256
